# attention sub-tiles: raised priority held from the QK MFMA run through the row-max tree and deferred-max test, dropped at the exponentials
# speedup vs baseline: 1.0069x; 1.0069x over previous
.LBB0_447:
	s_add_i32 s2, s26, s23
	s_and_b32 s3, s30, 0x18000
	s_add_i32 s3, s3, 0
	s_add_i32 s33, s3, s27
	v_add_u32_e32 v2, s33, v162
	v_add_u32_e32 v4, s33, v164
	v_add_u32_e32 v5, s33, v165
	v_add_u32_e32 v70, s33, v166
	s_ashr_i32 s33, s31, 2
	v_cvt_f32_i32_e32 v170, s33
	v_add_u32_e32 v106, s3, v160
	s_add_i32 s3, s2, 0x7e0
	v_add_u32_e32 v169, 0x4000, v106
	s_cmp_gt_i32 s3, s28
	v_add_u32_e32 v174, v2, v145
	v_add_u32_e32 v173, v4, v145
	v_add_u32_e32 v172, v5, v145
	v_add_u32_e32 v171, v70, v145
	s_barrier
	s_cbranch_scc1 .LBB0_455
	ds_read_b128 v[70:73], v174 offset:4096
	ds_read_b128 v[188:191], v173 offset:4096
	ds_read_b128 v[192:195], v172 offset:4096
	ds_read_b128 v[202:205], v171 offset:4096
	s_and_b32 s3, s3, 0xe0
	v_or_b32_e32 v2, s3, v159
	v_cvt_f32_ubyte0_e32 v2, v2
	v_and_b32_e32 v2, 0x7fff0000, v2
	v_or_b32_sdwa v2, v2, v170 dst_sel:DWORD dst_unused:UNUSED_PAD src0_sel:DWORD src1_sel:WORD_1
	v_cndmask_b32_e64 v2, 0, v2, s[36:37]
	v_mov_b32_e32 v4, v3
	s_waitcnt lgkmcnt(3)
	s_setprio 1
	v_mfma_f32_32x32x16_bf16 v[70:85], v[70:73], v[86:89], 0
	v_mov_b32_e32 v5, v3
	s_add_i32 s3, s2, 0x7ff
	s_cmp_ge_i32 s19, s3
	s_cselect_b64 s[40:41], -1, 0
	s_add_i32 s3, s29, 0xffffffa0
	s_cmp_lt_i32 s3, 0x3fffffe1
	v_add_u32_e32 v175, v169, v150
	s_waitcnt lgkmcnt(2)
	v_mfma_f32_32x32x16_bf16 v[70:85], v[188:191], v[90:93], v[70:85]
	s_cselect_b64 s[42:43], -1, 0
	s_and_b64 s[40:41], s[40:41], s[42:43]
	s_and_b64 vcc, exec, s[40:41]
	s_waitcnt lgkmcnt(1)
	v_mfma_f32_32x32x16_bf16 v[70:85], v[192:195], v[94:97], v[70:85]
	s_waitcnt lgkmcnt(0)
	v_mfma_f32_32x32x16_bf16 v[70:85], v[202:205], v[98:101], v[70:85]
	v_mfma_f32_32x32x16_bf16 v[70:85], v[2:5], v[102:105], v[70:85]
	v_add3_u32 v2, v106, v142, s68
	v_add_u32_e32 v4, v169, v146
	v_add_u32_e32 v5, v169, v148
	ds_read_b64_tr_b16 v[134:135], v2
	ds_read_b64_tr_b16 v[136:137], v2 offset:2048
	ds_read_b64_tr_b16 v[130:131], v4
	ds_read_b64_tr_b16 v[132:133], v4 offset:2048
	ds_read_b64_tr_b16 v[126:127], v5
	ds_read_b64_tr_b16 v[128:129], v5 offset:2048
	ds_read_b64_tr_b16 v[122:123], v175
	ds_read_b64_tr_b16 v[124:125], v175 offset:2048
	ds_read_b64_tr_b16 v[118:119], v2 offset:4096
	ds_read_b64_tr_b16 v[120:121], v2 offset:6144
	ds_read_b64_tr_b16 v[114:115], v4 offset:4096
	ds_read_b64_tr_b16 v[116:117], v4 offset:6144
	ds_read_b64_tr_b16 v[110:111], v5 offset:4096
	ds_read_b64_tr_b16 v[112:113], v5 offset:6144
	ds_read_b64_tr_b16 v[106:107], v175 offset:4096
	ds_read_b64_tr_b16 v[108:109], v175 offset:6144
	s_cbranch_vccnz .LBB0_452
	v_add_u32_e32 v2, s29, v161
	v_add_u32_e32 v4, 0xffffffa0, v2
	v_cmp_gt_u32_e32 vcc, 2.0, v4
	v_add_u32_e32 v4, s23, v163
	v_add_u32_e32 v4, 0x60, v4
	s_nop 2
	v_cndmask_b32_e32 v70, v197, v70, vcc
	v_cmp_lt_u32_e32 vcc, s75, v4
	v_add_u32_e32 v4, 0xffffff9e, v2
	s_nop 0
	v_cndmask_b32_e32 v71, v197, v71, vcc
	v_cmp_gt_u32_e32 vcc, 2.0, v4
	v_add_u32_e32 v4, 0xffffff9d, v2
	s_nop 0
	v_cndmask_b32_e32 v72, v197, v72, vcc
	v_cmp_gt_u32_e32 vcc, 2.0, v4
	v_add_u32_e32 v4, 0xffffff98, v2
	s_nop 0
	v_cndmask_b32_e32 v73, v197, v73, vcc
	v_cmp_gt_u32_e32 vcc, 2.0, v4
	v_add_u32_e32 v4, 0xffffff97, v2
	s_nop 0
	v_cndmask_b32_e32 v74, v197, v74, vcc
	v_cmp_gt_u32_e32 vcc, 2.0, v4
	v_add_u32_e32 v4, 0xffffff96, v2
	s_nop 0
	v_cndmask_b32_e32 v75, v197, v75, vcc
	v_cmp_gt_u32_e32 vcc, 2.0, v4
	v_add_u32_e32 v4, 0xffffff95, v2
	s_nop 0
	v_cndmask_b32_e32 v76, v197, v76, vcc
	v_cmp_gt_u32_e32 vcc, 2.0, v4
	v_add_u32_e32 v4, 0xffffff90, v2
	s_nop 0
	v_cndmask_b32_e32 v77, v197, v77, vcc
	v_cmp_gt_u32_e32 vcc, 2.0, v4
	v_add_u32_e32 v4, 0xffffff8f, v2
	s_nop 0
	v_cndmask_b32_e32 v78, v197, v78, vcc
	v_cmp_gt_u32_e32 vcc, 2.0, v4
	v_add_u32_e32 v4, 0xffffff8e, v2
	s_nop 0
	v_cndmask_b32_e32 v79, v197, v79, vcc
	v_cmp_gt_u32_e32 vcc, 2.0, v4
	v_add_u32_e32 v4, 0xffffff8d, v2
	s_nop 0
	v_cndmask_b32_e32 v80, v197, v80, vcc
	v_cmp_gt_u32_e32 vcc, 2.0, v4
	v_add_u32_e32 v4, 0xffffff88, v2
	s_nop 0
	v_cndmask_b32_e32 v81, v197, v81, vcc
	v_cmp_gt_u32_e32 vcc, 2.0, v4
	v_add_u32_e32 v4, 0xffffff87, v2
	s_nop 0
	v_cndmask_b32_e32 v82, v197, v82, vcc
	v_cmp_gt_u32_e32 vcc, 2.0, v4
	v_add_u32_e32 v4, 0xffffff86, v2
	v_add_u32_e32 v2, 0xffffff85, v2
	v_cndmask_b32_e32 v83, v197, v83, vcc
	v_cmp_gt_u32_e32 vcc, 2.0, v4
	s_nop 1
	v_cndmask_b32_e32 v84, v197, v84, vcc
	v_cmp_gt_u32_e32 vcc, 2.0, v2
	s_nop 1
	v_cndmask_b32_e32 v85, v197, v85, vcc

.LBB0_454:
	s_setprio 0
	v_mul_f32_e32 v2, 0xbfb8aa3b, v168
	v_fmamk_f32 v4, v70, 0x3fb8aa3b, v2
	v_fmamk_f32 v70, v72, 0x3fb8aa3b, v2
	v_exp_f32_e32 v176, v70
	v_fmamk_f32 v70, v73, 0x3fb8aa3b, v2
	v_exp_f32_e32 v177, v70
	v_fmamk_f32 v70, v74, 0x3fb8aa3b, v2
	v_exp_f32_e32 v74, v70
	v_fmamk_f32 v70, v75, 0x3fb8aa3b, v2
	v_exp_f32_e32 v75, v70
	v_fmamk_f32 v70, v76, 0x3fb8aa3b, v2
	v_fmamk_f32 v5, v71, 0x3fb8aa3b, v2
	v_exp_f32_e32 v76, v70
	v_fmamk_f32 v70, v77, 0x3fb8aa3b, v2
	v_exp_f32_e32 v4, v4
	v_exp_f32_e32 v5, v5
	v_exp_f32_e32 v77, v70
	v_cvt_pk_bf16_f32 v70, v4, v5
	v_cvt_pk_bf16_f32 v71, v176, v177
	v_cvt_pk_bf16_f32 v72, v74, v75
	v_cvt_pk_bf16_f32 v73, v76, v77
	v_fmamk_f32 v78, v78, 0x3fb8aa3b, v2
	s_waitcnt lgkmcnt(0)
	s_setprio 1
	v_mfma_f32_32x32x16_bf16 v[54:69], v[134:137], v[70:73], v[54:69]
	v_fmamk_f32 v79, v79, 0x3fb8aa3b, v2
	v_exp_f32_e32 v78, v78
	v_exp_f32_e32 v79, v79
	v_fmamk_f32 v80, v80, 0x3fb8aa3b, v2
	v_fmamk_f32 v81, v81, 0x3fb8aa3b, v2
	v_pk_add_f32 v[4:5], v[4:5], 0 op_sel_hi:[1,0]
	v_exp_f32_e32 v80, v80
	v_mfma_f32_32x32x16_bf16 v[38:53], v[130:133], v[70:73], v[38:53]
	v_exp_f32_e32 v81, v81
	v_fmamk_f32 v82, v82, 0x3fb8aa3b, v2
	v_fmamk_f32 v83, v83, 0x3fb8aa3b, v2
	v_fmamk_f32 v84, v84, 0x3fb8aa3b, v2
	v_fmac_f32_e32 v2, 0x3fb8aa3b, v85
	v_pk_add_f32 v[4:5], v[176:177], v[4:5]
	v_exp_f32_e32 v82, v82
	v_mfma_f32_32x32x16_bf16 v[22:37], v[126:129], v[70:73], v[22:37]
	v_exp_f32_e32 v83, v83
	v_exp_f32_e32 v84, v84
	v_exp_f32_e32 v85, v2
	v_pk_add_f32 v[4:5], v[74:75], v[4:5]
	s_nop 0
	v_pk_add_f32 v[4:5], v[76:77], v[4:5]
	v_mfma_f32_32x32x16_bf16 v[6:21], v[122:125], v[70:73], v[6:21]
	v_cvt_pk_bf16_f32 v70, v78, v79
	v_cvt_pk_bf16_f32 v71, v80, v81
	v_cvt_pk_bf16_f32 v72, v82, v83
	v_cvt_pk_bf16_f32 v73, v84, v85
	v_add_f32_e64 v4, v78, v4
	v_add_f32_e64 v5, v79, v5
	v_add_f32_e64 v4, v80, v4
	v_add_f32_e64 v5, v81, v5
	v_mfma_f32_32x32x16_bf16 v[54:69], v[118:121], v[70:73], v[54:69]
	v_add_f32_e64 v4, v82, v4
	v_add_f32_e64 v5, v83, v5
	v_add_f32_e64 v4, v84, v4
	v_add_f32_e64 v5, v85, v5
	v_add_f32_e32 v2, v4, v5
	v_add_f32_e32 v167, v167, v2
	v_mfma_f32_32x32x16_bf16 v[38:53], v[114:117], v[70:73], v[38:53]
	v_mfma_f32_32x32x16_bf16 v[22:37], v[110:113], v[70:73], v[22:37]
	v_mfma_f32_32x32x16_bf16 v[6:21], v[106:109], v[70:73], v[6:21]
	s_setprio 0

.Lring_issue_skip_2:
	s_add_i32 s3, s2, 0x7c0
	s_cmp_gt_i32 s3, s28
	s_cbranch_scc1 .LBB0_461
	ds_read_b128 v[70:73], v174
	ds_read_b128 v[188:191], v173
	ds_read_b128 v[192:195], v172
	ds_read_b128 v[202:205], v171
	s_and_b32 s3, s3, 0xc0
	v_or_b32_e32 v2, s3, v159
	v_cvt_f32_ubyte0_e32 v2, v2
	v_and_b32_e32 v2, 0x7fff0000, v2
	v_or_b32_sdwa v2, v2, v170 dst_sel:DWORD dst_unused:UNUSED_PAD src0_sel:DWORD src1_sel:WORD_1
	v_cndmask_b32_e64 v2, 0, v2, s[36:37]
	v_mov_b32_e32 v4, v3
	s_waitcnt lgkmcnt(3)
	s_setprio 1
	v_mfma_f32_32x32x16_bf16 v[70:85], v[70:73], v[86:89], 0
	v_mov_b32_e32 v5, v3
	s_addk_i32 s2, 0x7df
	s_cmp_ge_i32 s19, s2
	s_cselect_b64 s[2:3], -1, 0
	s_sub_i32 s33, s29, 64
	s_cmp_lt_i32 s33, 0x3fffffe1
	s_cselect_b64 s[40:41], -1, 0
	s_waitcnt lgkmcnt(2)
	v_mfma_f32_32x32x16_bf16 v[70:85], v[188:191], v[90:93], v[70:85]
	s_and_b64 s[2:3], s[2:3], s[40:41]
	s_and_b64 vcc, exec, s[2:3]
	s_waitcnt lgkmcnt(1)
	v_mfma_f32_32x32x16_bf16 v[70:85], v[192:195], v[94:97], v[70:85]
	s_waitcnt lgkmcnt(0)
	v_mfma_f32_32x32x16_bf16 v[70:85], v[202:205], v[98:101], v[70:85]
	v_mfma_f32_32x32x16_bf16 v[70:85], v[2:5], v[102:105], v[70:85]
	v_add_u32_e32 v2, v169, v142
	v_add_u32_e32 v4, v169, v152
	v_add_u32_e32 v5, v169, v154
	v_add_u32_e32 v169, v169, v156
	ds_read_b64_tr_b16 v[134:135], v2
	ds_read_b64_tr_b16 v[136:137], v2 offset:2048
	ds_read_b64_tr_b16 v[130:131], v4
	ds_read_b64_tr_b16 v[132:133], v4 offset:2048
	ds_read_b64_tr_b16 v[126:127], v5
	ds_read_b64_tr_b16 v[128:129], v5 offset:2048
	ds_read_b64_tr_b16 v[122:123], v169
	ds_read_b64_tr_b16 v[124:125], v169 offset:2048
	ds_read_b64_tr_b16 v[118:119], v2 offset:4096
	ds_read_b64_tr_b16 v[120:121], v2 offset:6144
	ds_read_b64_tr_b16 v[114:115], v4 offset:4096
	ds_read_b64_tr_b16 v[116:117], v4 offset:6144
	ds_read_b64_tr_b16 v[110:111], v5 offset:4096
	ds_read_b64_tr_b16 v[112:113], v5 offset:6144
	ds_read_b64_tr_b16 v[106:107], v169 offset:4096
	ds_read_b64_tr_b16 v[108:109], v169 offset:6144
	s_cbranch_vccnz .LBB0_458
	v_add_u32_e32 v2, s29, v161
	v_subrev_u32_e32 v4, 64, v2
	v_cmp_gt_u32_e32 vcc, 2.0, v4
	v_add3_u32 v4, v163, s23, 64
	s_nop 2
	v_cndmask_b32_e32 v70, v197, v70, vcc
	v_cmp_lt_u32_e32 vcc, s75, v4
	v_add_u32_e32 v4, 0xffffffbe, v2
	s_nop 0
	v_cndmask_b32_e32 v71, v197, v71, vcc
	v_cmp_gt_u32_e32 vcc, 2.0, v4
	v_add_u32_e32 v4, 0xffffffbd, v2
	s_nop 0
	v_cndmask_b32_e32 v72, v197, v72, vcc
	v_cmp_gt_u32_e32 vcc, 2.0, v4
	v_add_u32_e32 v4, 0xffffffb8, v2
	s_nop 0
	v_cndmask_b32_e32 v73, v197, v73, vcc
	v_cmp_gt_u32_e32 vcc, 2.0, v4
	v_add_u32_e32 v4, 0xffffffb7, v2
	s_nop 0
	v_cndmask_b32_e32 v74, v197, v74, vcc
	v_cmp_gt_u32_e32 vcc, 2.0, v4
	v_add_u32_e32 v4, 0xffffffb6, v2
	s_nop 0
	v_cndmask_b32_e32 v75, v197, v75, vcc
	v_cmp_gt_u32_e32 vcc, 2.0, v4
	v_add_u32_e32 v4, 0xffffffb5, v2
	s_nop 0
	v_cndmask_b32_e32 v76, v197, v76, vcc
	v_cmp_gt_u32_e32 vcc, 2.0, v4
	v_add_u32_e32 v4, 0xffffffb0, v2
	s_nop 0
	v_cndmask_b32_e32 v77, v197, v77, vcc
	v_cmp_gt_u32_e32 vcc, 2.0, v4
	v_add_u32_e32 v4, 0xffffffaf, v2
	s_nop 0
	v_cndmask_b32_e32 v78, v197, v78, vcc
	v_cmp_gt_u32_e32 vcc, 2.0, v4
	v_add_u32_e32 v4, 0xffffffae, v2
	s_nop 0
	v_cndmask_b32_e32 v79, v197, v79, vcc
	v_cmp_gt_u32_e32 vcc, 2.0, v4
	v_add_u32_e32 v4, 0xffffffad, v2
	s_nop 0
	v_cndmask_b32_e32 v80, v197, v80, vcc
	v_cmp_gt_u32_e32 vcc, 2.0, v4
	v_add_u32_e32 v4, 0xffffffa8, v2
	s_nop 0
	v_cndmask_b32_e32 v81, v197, v81, vcc
	v_cmp_gt_u32_e32 vcc, 2.0, v4
	v_add_u32_e32 v4, 0xffffffa7, v2
	s_nop 0
	v_cndmask_b32_e32 v82, v197, v82, vcc
	v_cmp_gt_u32_e32 vcc, 2.0, v4
	v_add_u32_e32 v4, 0xffffffa6, v2
	v_add_u32_e32 v2, 0xffffffa5, v2
	v_cndmask_b32_e32 v83, v197, v83, vcc
	v_cmp_gt_u32_e32 vcc, 2.0, v4
	s_nop 1
	v_cndmask_b32_e32 v84, v197, v84, vcc
	v_cmp_gt_u32_e32 vcc, 2.0, v2
	s_nop 1
	v_cndmask_b32_e32 v85, v197, v85, vcc

.LBB0_460:
	s_setprio 0
	v_mul_f32_e32 v2, 0xbfb8aa3b, v168
	v_fmamk_f32 v4, v70, 0x3fb8aa3b, v2
	v_fmamk_f32 v70, v72, 0x3fb8aa3b, v2
	v_exp_f32_e32 v170, v70
	v_fmamk_f32 v70, v73, 0x3fb8aa3b, v2
	v_exp_f32_e32 v171, v70
	v_fmamk_f32 v70, v74, 0x3fb8aa3b, v2
	v_exp_f32_e32 v74, v70
	v_fmamk_f32 v70, v75, 0x3fb8aa3b, v2
	v_exp_f32_e32 v75, v70
	v_fmamk_f32 v70, v76, 0x3fb8aa3b, v2
	v_fmamk_f32 v5, v71, 0x3fb8aa3b, v2
	v_exp_f32_e32 v76, v70
	v_fmamk_f32 v70, v77, 0x3fb8aa3b, v2
	v_exp_f32_e32 v4, v4
	v_exp_f32_e32 v5, v5
	v_exp_f32_e32 v77, v70
	v_cvt_pk_bf16_f32 v70, v4, v5
	v_cvt_pk_bf16_f32 v71, v170, v171
	v_cvt_pk_bf16_f32 v72, v74, v75
	v_cvt_pk_bf16_f32 v73, v76, v77
	v_fmamk_f32 v78, v78, 0x3fb8aa3b, v2
	s_waitcnt lgkmcnt(0)
	s_setprio 1
	v_mfma_f32_32x32x16_bf16 v[54:69], v[134:137], v[70:73], v[54:69]
	v_fmamk_f32 v79, v79, 0x3fb8aa3b, v2
	v_exp_f32_e32 v78, v78
	v_exp_f32_e32 v79, v79
	v_fmamk_f32 v80, v80, 0x3fb8aa3b, v2
	v_fmamk_f32 v81, v81, 0x3fb8aa3b, v2
	v_pk_add_f32 v[4:5], v[4:5], 0 op_sel_hi:[1,0]
	v_exp_f32_e32 v80, v80
	v_mfma_f32_32x32x16_bf16 v[38:53], v[130:133], v[70:73], v[38:53]
	v_exp_f32_e32 v81, v81
	v_fmamk_f32 v82, v82, 0x3fb8aa3b, v2
	v_fmamk_f32 v83, v83, 0x3fb8aa3b, v2
	v_fmamk_f32 v84, v84, 0x3fb8aa3b, v2
	v_fmac_f32_e32 v2, 0x3fb8aa3b, v85
	v_pk_add_f32 v[4:5], v[170:171], v[4:5]
	v_exp_f32_e32 v82, v82
	v_mfma_f32_32x32x16_bf16 v[22:37], v[126:129], v[70:73], v[22:37]
	v_exp_f32_e32 v83, v83
	v_exp_f32_e32 v84, v84
	v_exp_f32_e32 v85, v2
	v_pk_add_f32 v[4:5], v[74:75], v[4:5]
	s_nop 0
	v_pk_add_f32 v[4:5], v[76:77], v[4:5]
	v_mfma_f32_32x32x16_bf16 v[6:21], v[122:125], v[70:73], v[6:21]
	v_cvt_pk_bf16_f32 v70, v78, v79
	v_cvt_pk_bf16_f32 v71, v80, v81
	v_cvt_pk_bf16_f32 v72, v82, v83
	v_cvt_pk_bf16_f32 v73, v84, v85
	v_add_f32_e64 v4, v78, v4
	v_add_f32_e64 v5, v79, v5
	v_add_f32_e64 v4, v80, v4
	v_add_f32_e64 v5, v81, v5
	v_mfma_f32_32x32x16_bf16 v[54:69], v[118:121], v[70:73], v[54:69]
	v_add_f32_e64 v4, v82, v4
	v_add_f32_e64 v5, v83, v5
	v_add_f32_e64 v4, v84, v4
	v_add_f32_e64 v5, v85, v5
	v_add_f32_e32 v2, v4, v5
	v_add_f32_e32 v167, v167, v2
	v_mfma_f32_32x32x16_bf16 v[38:53], v[114:117], v[70:73], v[38:53]
	v_mfma_f32_32x32x16_bf16 v[22:37], v[110:113], v[70:73], v[22:37]
	v_mfma_f32_32x32x16_bf16 v[6:21], v[106:109], v[70:73], v[6:21]
	s_setprio 0

.LBB0_509:
	s_setprio 0
	v_mul_f32_e32 v2, 0xbfb8aa3b, v110
	v_fmamk_f32 v16, v50, 0x3fb8aa3b, v2
	v_fmamk_f32 v50, v52, 0x3fb8aa3b, v2
	v_exp_f32_e32 v52, v50
	v_fmamk_f32 v50, v53, 0x3fb8aa3b, v2
	v_exp_f32_e32 v53, v50
	v_fmamk_f32 v50, v54, 0x3fb8aa3b, v2
	v_exp_f32_e32 v54, v50
	v_fmamk_f32 v50, v55, 0x3fb8aa3b, v2
	v_exp_f32_e32 v55, v50
	v_fmamk_f32 v50, v56, 0x3fb8aa3b, v2
	v_exp_f32_e32 v56, v50
	v_fmamk_f32 v50, v57, 0x3fb8aa3b, v2
	v_exp_f32_e32 v57, v50
	v_fmamk_f32 v50, v58, 0x3fb8aa3b, v2
	v_exp_f32_e32 v58, v50
	v_fmamk_f32 v50, v59, 0x3fb8aa3b, v2
	v_fmamk_f32 v17, v51, 0x3fb8aa3b, v2
	v_exp_f32_e32 v59, v50
	v_fmamk_f32 v50, v60, 0x3fb8aa3b, v2
	v_exp_f32_e32 v16, v16
	v_exp_f32_e32 v17, v17
	v_exp_f32_e32 v60, v50
	v_fmamk_f32 v50, v61, 0x3fb8aa3b, v2
	v_exp_f32_e32 v61, v50
	v_fmamk_f32 v50, v62, 0x3fb8aa3b, v2
	v_exp_f32_e32 v62, v50
	v_fmamk_f32 v50, v63, 0x3fb8aa3b, v2
	v_exp_f32_e32 v63, v50
	v_fmamk_f32 v50, v64, 0x3fb8aa3b, v2
	v_exp_f32_e32 v64, v50
	v_fmac_f32_e32 v2, 0x3fb8aa3b, v65
	v_pk_add_f32 v[50:51], v[16:17], v[52:53]
	v_exp_f32_e32 v65, v2
	v_pk_add_f32 v[244:245], v[54:55], v[56:57]
	v_pk_add_f32 v[50:51], v[58:59], v[50:51]
	v_pk_add_f32 v[244:245], v[60:61], v[244:245]
	v_pk_add_f32 v[50:51], v[62:63], v[50:51]
	v_pk_add_f32 v[244:245], v[64:65], v[244:245]
	s_nop 0
	v_pk_add_f32 v[50:51], v[50:51], v[244:245]
	s_nop 0
	v_add_f32_e32 v2, v50, v51
	v_cvt_pk_bf16_f32 v50, v16, v17
	v_cvt_pk_bf16_f32 v51, v52, v53
	v_cvt_pk_bf16_f32 v52, v54, v55
	v_cvt_pk_bf16_f32 v53, v56, v57
	v_add_f32_e32 v107, v107, v2
	s_waitcnt lgkmcnt(0)
	s_setprio 1
	v_mfma_f32_32x32x16_bf16 v[34:49], v[86:89], v[50:53], v[34:49]
	v_mfma_f32_32x32x16_bf16 v[18:33], v[12:15], v[50:53], v[18:33]
	v_cvt_pk_bf16_f32 v12, v58, v59
	v_cvt_pk_bf16_f32 v13, v60, v61
	v_cvt_pk_bf16_f32 v14, v62, v63
	v_cvt_pk_bf16_f32 v15, v64, v65
	s_nop 0
	v_mfma_f32_32x32x16_bf16 v[34:49], v[8:11], v[12:15], v[34:49]
	v_mfma_f32_32x32x16_bf16 v[18:33], v[4:7], v[12:15], v[18:33]
	s_setprio 0

.Lw_win_4_done:
.LBB0_519:
	s_cmp_eq_u32 s32, 0
	s_cselect_b32 s84, 0, 1
	s_sub_u32 s32, s32, s84
	s_add_i32 s2, s29, s22
	s_add_i32 s3, s27, s21
	s_add_i32 s3, s3, -1
	s_and_b32 s31, s30, 0xc000
	s_add_i32 s33, s31, 0
	s_ashr_i32 s3, s3, 2
	s_add_i32 s31, s2, 0x7e0
	s_cmp_gt_i32 s31, s23
	v_cvt_f32_i32_e32 v111, s3
	s_cselect_b64 s[34:35], -1, 0
	s_add_i32 s3, s2, 0x7ff
	s_cmp_lt_i32 s3, s24
	s_cselect_b64 s[38:39], -1, 0
	v_add_u32_e32 v2, s33, v101
	v_add_u32_e32 v4, s33, v102
	v_add_u32_e32 v5, s33, v103
	v_add_u32_e32 v6, s33, v104
	s_or_b64 s[34:35], s[34:35], s[38:39]
	s_and_b64 vcc, exec, s[34:35]
	v_add_u32_e32 v115, v2, v100
	v_add_u32_e32 v114, v4, v100
	v_add_u32_e32 v113, v5, v100
	v_add_u32_e32 v112, v6, v100
	v_add_u32_e32 v16, s33, v105
	v_add_u32_e32 v17, s33, v106
	s_barrier
	s_cbranch_vccnz .LBB0_527
	ds_read_b128 v[4:7], v115 offset:4096
	ds_read_b128 v[188:191], v114 offset:4096
	ds_read_b128 v[192:195], v113 offset:4096
	ds_read_b128 v[202:205], v112 offset:4096
	s_and_b32 s31, s31, 0xe0
	v_or_b32_e32 v2, s31, v99
	v_cvt_f32_ubyte0_e32 v2, v2
	v_and_b32_e32 v2, 0x7fff0000, v2
	v_or_b32_sdwa v2, v2, v111 dst_sel:DWORD dst_unused:UNUSED_PAD src0_sel:DWORD src1_sel:WORD_1
	v_cndmask_b32_e64 v246, 0, v2, s[36:37]
	s_cmp_ge_i32 s20, s3
	s_cselect_b64 s[34:35], -1, 0
	s_waitcnt lgkmcnt(3)
	s_setprio 1
	v_mfma_f32_32x32x16_bf16 v[50:65], v[4:7], v[74:77], 0
	s_sub_i32 s3, s19, 32
	s_cmpk_lt_i32 s3, 0x1e1
	v_add3_u32 v116, v17, v94, s69
	s_cselect_b64 s[38:39], -1, 0
	s_and_b64 s[34:35], s[34:35], s[38:39]
	s_and_b64 vcc, exec, s[34:35]
	s_waitcnt lgkmcnt(2)
	v_mfma_f32_32x32x16_bf16 v[50:65], v[188:191], v[66:69], v[50:65]
	s_waitcnt lgkmcnt(1)
	v_mfma_f32_32x32x16_bf16 v[50:65], v[192:195], v[70:73], v[50:65]
	s_waitcnt lgkmcnt(0)
	v_mfma_f32_32x32x16_bf16 v[50:65], v[202:205], v[78:81], v[50:65]
	v_mfma_f32_32x32x16_bf16 v[50:65], v[246:249], v[82:85], v[50:65]
	v_add3_u32 v2, v16, v94, s69
	ds_read_b64_tr_b16 v[86:87], v2
	ds_read_b64_tr_b16 v[88:89], v2 offset:1024
	ds_read_b64_tr_b16 v[12:13], v116
	ds_read_b64_tr_b16 v[14:15], v116 offset:1024
	ds_read_b64_tr_b16 v[8:9], v2 offset:2048
	ds_read_b64_tr_b16 v[10:11], v2 offset:3072
	ds_read_b64_tr_b16 v[4:5], v116 offset:2048
	ds_read_b64_tr_b16 v[6:7], v116 offset:3072
	s_cbranch_vccnz .LBB0_524
	v_add_u32_e32 v2, s19, v108
	v_subrev_u32_e32 v116, 32, v2
	v_cmp_gt_u32_e32 vcc, s79, v116
	v_add3_u32 v116, v109, s22, 32
	s_nop 5
	v_cndmask_b32_e32 v50, v197, v50, vcc
	v_cmp_lt_u32_e32 vcc, s80, v116
	v_subrev_u32_e32 v116, 34, v2
	s_nop 0
	v_cndmask_b32_e32 v51, v197, v51, vcc
	v_cmp_gt_u32_e32 vcc, s79, v116
	v_subrev_u32_e32 v116, 35, v2
	s_nop 0
	v_cndmask_b32_e32 v52, v197, v52, vcc
	v_cmp_gt_u32_e32 vcc, s79, v116
	v_subrev_u32_e32 v116, 40, v2
	s_nop 0
	v_cndmask_b32_e32 v53, v197, v53, vcc
	v_cmp_gt_u32_e32 vcc, s79, v116
	v_subrev_u32_e32 v116, 41, v2
	s_nop 0
	v_cndmask_b32_e32 v54, v197, v54, vcc
	v_cmp_gt_u32_e32 vcc, s79, v116
	v_subrev_u32_e32 v116, 42, v2
	s_nop 0
	v_cndmask_b32_e32 v55, v197, v55, vcc
	v_cmp_gt_u32_e32 vcc, s79, v116
	v_subrev_u32_e32 v116, 43, v2
	s_nop 0
	v_cndmask_b32_e32 v56, v197, v56, vcc
	v_cmp_gt_u32_e32 vcc, s79, v116
	v_subrev_u32_e32 v116, 48, v2
	s_nop 0
	v_cndmask_b32_e32 v57, v197, v57, vcc
	v_cmp_gt_u32_e32 vcc, s79, v116
	v_subrev_u32_e32 v116, 49, v2
	s_nop 0
	v_cndmask_b32_e32 v58, v197, v58, vcc
	v_cmp_gt_u32_e32 vcc, s79, v116
	v_subrev_u32_e32 v116, 50, v2
	s_nop 0
	v_cndmask_b32_e32 v59, v197, v59, vcc
	v_cmp_gt_u32_e32 vcc, s79, v116
	v_subrev_u32_e32 v116, 51, v2
	s_nop 0
	v_cndmask_b32_e32 v60, v197, v60, vcc
	v_cmp_gt_u32_e32 vcc, s79, v116
	v_subrev_u32_e32 v116, 56, v2
	s_nop 0
	v_cndmask_b32_e32 v61, v197, v61, vcc
	v_cmp_gt_u32_e32 vcc, s79, v116
	v_subrev_u32_e32 v116, 57, v2
	s_nop 0
	v_cndmask_b32_e32 v62, v197, v62, vcc
	v_cmp_gt_u32_e32 vcc, s79, v116
	v_subrev_u32_e32 v116, 58, v2
	v_subrev_u32_e32 v2, 59, v2
	v_cndmask_b32_e32 v63, v197, v63, vcc
	v_cmp_gt_u32_e32 vcc, s79, v116
	s_nop 1
	v_cndmask_b32_e32 v64, v197, v64, vcc
	v_cmp_gt_u32_e32 vcc, s79, v2
	s_nop 1
	v_cndmask_b32_e32 v65, v197, v65, vcc

.LBB0_526:
	s_setprio 0
	v_mul_f32_e32 v2, 0xbfb8aa3b, v110
	v_fmamk_f32 v50, v50, 0x3fb8aa3b, v2
	v_fmamk_f32 v51, v51, 0x3fb8aa3b, v2
	v_exp_f32_e32 v50, v50
	v_exp_f32_e32 v51, v51
	v_fmamk_f32 v52, v52, 0x3fb8aa3b, v2
	v_fmamk_f32 v53, v53, 0x3fb8aa3b, v2
	v_exp_f32_e32 v52, v52
	v_exp_f32_e32 v53, v53
	v_fmamk_f32 v54, v54, 0x3fb8aa3b, v2
	v_fmamk_f32 v55, v55, 0x3fb8aa3b, v2
	v_fmamk_f32 v56, v56, 0x3fb8aa3b, v2
	v_fmamk_f32 v57, v57, 0x3fb8aa3b, v2
	v_pk_add_f32 v[116:117], v[50:51], 0 op_sel_hi:[1,0]
	v_exp_f32_e32 v54, v54
	v_exp_f32_e32 v55, v55
	v_exp_f32_e32 v56, v56
	v_exp_f32_e32 v57, v57
	v_pk_add_f32 v[116:117], v[52:53], v[116:117]
	v_cvt_pk_bf16_f32 v50, v50, v51
	v_cvt_pk_bf16_f32 v51, v52, v53
	v_cvt_pk_bf16_f32 v52, v54, v55
	v_cvt_pk_bf16_f32 v53, v56, v57
	v_fmamk_f32 v58, v58, 0x3fb8aa3b, v2
	s_waitcnt lgkmcnt(0)
	s_setprio 1
	v_mfma_f32_32x32x16_bf16 v[34:49], v[86:89], v[50:53], v[34:49]
	v_fmamk_f32 v59, v59, 0x3fb8aa3b, v2
	v_exp_f32_e32 v58, v58
	v_exp_f32_e32 v59, v59
	v_fmamk_f32 v60, v60, 0x3fb8aa3b, v2
	v_fmamk_f32 v61, v61, 0x3fb8aa3b, v2
	v_exp_f32_e32 v60, v60
	v_exp_f32_e32 v61, v61
	v_mfma_f32_32x32x16_bf16 v[18:33], v[12:15], v[50:53], v[18:33]
	v_fmamk_f32 v62, v62, 0x3fb8aa3b, v2
	v_fmamk_f32 v63, v63, 0x3fb8aa3b, v2
	v_fmamk_f32 v64, v64, 0x3fb8aa3b, v2
	v_fmac_f32_e32 v2, 0x3fb8aa3b, v65
	v_exp_f32_e32 v62, v62
	v_exp_f32_e32 v63, v63
	v_exp_f32_e32 v64, v64
	v_exp_f32_e32 v65, v2
	v_pk_add_f32 v[116:117], v[54:55], v[116:117]
	v_cvt_pk_bf16_f32 v12, v58, v59
	v_cvt_pk_bf16_f32 v13, v60, v61
	v_cvt_pk_bf16_f32 v14, v62, v63
	v_cvt_pk_bf16_f32 v15, v64, v65
	s_nop 0
	v_mfma_f32_32x32x16_bf16 v[34:49], v[8:11], v[12:15], v[34:49]
	v_add_f32_e64 v116, v56, v116
	v_add_f32_e64 v117, v57, v117
	v_add_f32_e64 v116, v58, v116
	v_add_f32_e64 v117, v59, v117
	v_add_f32_e64 v116, v60, v116
	v_add_f32_e64 v117, v61, v117
	v_pk_add_f32 v[116:117], v[62:63], v[116:117]
	v_mfma_f32_32x32x16_bf16 v[18:33], v[4:7], v[12:15], v[18:33]
	s_setprio 0
	v_add_f32_e64 v116, v64, v116
	v_add_f32_e64 v117, v65, v117
	v_add_f32_e32 v2, v116, v117
	v_add_f32_e32 v107, v107, v2

.Lring_issue_skip_0:
	s_add_i32 s3, s2, 0x7c0
	s_cmp_gt_i32 s3, s23
	s_cselect_b64 s[34:35], -1, 0
	s_addk_i32 s2, 0x7df
	s_cmp_lt_i32 s2, s24
	s_cselect_b64 s[38:39], -1, 0
	s_or_b64 s[34:35], s[34:35], s[38:39]
	s_and_b64 vcc, exec, s[34:35]
	s_cbranch_vccnz .LBB0_510
	ds_read_b128 v[4:7], v115
	ds_read_b128 v[188:191], v114
	ds_read_b128 v[192:195], v113
	ds_read_b128 v[202:205], v112
	s_and_b32 s3, s3, 0xc0
	v_or_b32_e32 v2, s3, v99
	v_cvt_f32_ubyte0_e32 v2, v2
	v_and_b32_e32 v2, 0x7fff0000, v2
	v_or_b32_sdwa v2, v2, v111 dst_sel:DWORD dst_unused:UNUSED_PAD src0_sel:DWORD src1_sel:WORD_1
	v_cndmask_b32_e64 v246, 0, v2, s[36:37]
	s_cmp_ge_i32 s20, s2
	s_cselect_b64 s[2:3], -1, 0
	s_waitcnt lgkmcnt(3)
	s_setprio 1
	v_mfma_f32_32x32x16_bf16 v[50:65], v[4:7], v[74:77], 0
	s_cmpk_lt_i32 s19, 0x1e1
	s_cselect_b64 s[34:35], -1, 0
	s_and_b64 s[2:3], s[2:3], s[34:35]
	s_and_b64 vcc, exec, s[2:3]
	s_waitcnt lgkmcnt(2)
	v_mfma_f32_32x32x16_bf16 v[50:65], v[188:191], v[66:69], v[50:65]
	s_waitcnt lgkmcnt(1)
	v_mfma_f32_32x32x16_bf16 v[50:65], v[192:195], v[70:73], v[50:65]
	s_waitcnt lgkmcnt(0)
	v_mfma_f32_32x32x16_bf16 v[50:65], v[202:205], v[78:81], v[50:65]
	v_mfma_f32_32x32x16_bf16 v[50:65], v[246:249], v[82:85], v[50:65]
	v_add3_u32 v2, v16, v94, s67
	v_add3_u32 v16, v17, v94, s67
	ds_read_b64_tr_b16 v[86:87], v2
	ds_read_b64_tr_b16 v[88:89], v2 offset:1024
	ds_read_b64_tr_b16 v[12:13], v16
	ds_read_b64_tr_b16 v[14:15], v16 offset:1024
	ds_read_b64_tr_b16 v[8:9], v2 offset:2048
	ds_read_b64_tr_b16 v[10:11], v2 offset:3072
	ds_read_b64_tr_b16 v[4:5], v16 offset:2048
	ds_read_b64_tr_b16 v[6:7], v16 offset:3072
	s_cbranch_vccnz .LBB0_530
	v_add_u32_e32 v2, s19, v108
	v_cmp_gt_u32_e32 vcc, s79, v2
	v_add_u32_e32 v16, s22, v109
	s_nop 5
	v_cndmask_b32_e32 v50, v197, v50, vcc
	v_cmp_lt_u32_e32 vcc, s80, v16
	v_add_u32_e32 v16, -2, v2
	s_nop 0
	v_cndmask_b32_e32 v51, v197, v51, vcc
	v_cmp_gt_u32_e32 vcc, s79, v16
	v_add_u32_e32 v16, -3, v2
	s_nop 0
	v_cndmask_b32_e32 v52, v197, v52, vcc
	v_cmp_gt_u32_e32 vcc, s79, v16
	v_add_u32_e32 v16, -8, v2
	s_nop 0
	v_cndmask_b32_e32 v53, v197, v53, vcc
	v_cmp_gt_u32_e32 vcc, s79, v16
	v_add_u32_e32 v16, -9, v2
	s_nop 0
	v_cndmask_b32_e32 v54, v197, v54, vcc
	v_cmp_gt_u32_e32 vcc, s79, v16
	v_add_u32_e32 v16, -10, v2
	s_nop 0
	v_cndmask_b32_e32 v55, v197, v55, vcc
	v_cmp_gt_u32_e32 vcc, s79, v16
	v_add_u32_e32 v16, -11, v2
	s_nop 0
	v_cndmask_b32_e32 v56, v197, v56, vcc
	v_cmp_gt_u32_e32 vcc, s79, v16
	v_add_u32_e32 v16, -16, v2
	s_nop 0
	v_cndmask_b32_e32 v57, v197, v57, vcc
	v_cmp_gt_u32_e32 vcc, s79, v16
	v_subrev_u32_e32 v16, 17, v2
	s_nop 0
	v_cndmask_b32_e32 v58, v197, v58, vcc
	v_cmp_gt_u32_e32 vcc, s79, v16
	v_subrev_u32_e32 v16, 18, v2
	s_nop 0
	v_cndmask_b32_e32 v59, v197, v59, vcc
	v_cmp_gt_u32_e32 vcc, s79, v16
	v_subrev_u32_e32 v16, 19, v2
	s_nop 0
	v_cndmask_b32_e32 v60, v197, v60, vcc
	v_cmp_gt_u32_e32 vcc, s79, v16
	v_subrev_u32_e32 v16, 24, v2
	s_nop 0
	v_cndmask_b32_e32 v61, v197, v61, vcc
	v_cmp_gt_u32_e32 vcc, s79, v16
	v_subrev_u32_e32 v16, 25, v2
	s_nop 0
	v_cndmask_b32_e32 v62, v197, v62, vcc
	v_cmp_gt_u32_e32 vcc, s79, v16
	v_subrev_u32_e32 v16, 26, v2
	v_subrev_u32_e32 v2, 27, v2
	v_cndmask_b32_e32 v63, v197, v63, vcc
	v_cmp_gt_u32_e32 vcc, s79, v16
	s_nop 1
	v_cndmask_b32_e32 v64, v197, v64, vcc
	v_cmp_gt_u32_e32 vcc, s79, v2
	s_nop 1
	v_cndmask_b32_e32 v65, v197, v65, vcc

.LBB0_668:
	s_setprio 0
	v_mul_f32_e32 v2, 0xbfb8aa3b, v158
	v_fmamk_f32 v16, v82, 0x3fb8aa3b, v2
	v_fmamk_f32 v82, v84, 0x3fb8aa3b, v2
	v_exp_f32_e32 v84, v82
	v_fmamk_f32 v82, v85, 0x3fb8aa3b, v2
	v_exp_f32_e32 v85, v82
	v_fmamk_f32 v82, v86, 0x3fb8aa3b, v2
	v_exp_f32_e32 v86, v82
	v_fmamk_f32 v82, v87, 0x3fb8aa3b, v2
	v_exp_f32_e32 v87, v82
	v_fmamk_f32 v82, v88, 0x3fb8aa3b, v2
	v_exp_f32_e32 v88, v82
	v_fmamk_f32 v82, v89, 0x3fb8aa3b, v2
	v_exp_f32_e32 v89, v82
	v_fmamk_f32 v82, v90, 0x3fb8aa3b, v2
	v_exp_f32_e32 v90, v82
	v_fmamk_f32 v82, v91, 0x3fb8aa3b, v2
	v_fmamk_f32 v17, v83, 0x3fb8aa3b, v2
	v_exp_f32_e32 v91, v82
	v_fmamk_f32 v82, v92, 0x3fb8aa3b, v2
	v_exp_f32_e32 v16, v16
	v_exp_f32_e32 v17, v17
	v_exp_f32_e32 v92, v82
	v_fmamk_f32 v82, v93, 0x3fb8aa3b, v2
	v_exp_f32_e32 v93, v82
	v_fmamk_f32 v82, v94, 0x3fb8aa3b, v2
	v_exp_f32_e32 v94, v82
	v_fmamk_f32 v82, v95, 0x3fb8aa3b, v2
	v_exp_f32_e32 v95, v82
	v_fmamk_f32 v82, v96, 0x3fb8aa3b, v2
	v_exp_f32_e32 v96, v82
	v_fmac_f32_e32 v2, 0x3fb8aa3b, v97
	v_pk_add_f32 v[82:83], v[16:17], v[84:85]
	v_exp_f32_e32 v97, v2
	v_pk_add_f32 v[218:219], v[86:87], v[88:89]
	v_pk_add_f32 v[82:83], v[90:91], v[82:83]
	v_pk_add_f32 v[218:219], v[92:93], v[218:219]
	v_pk_add_f32 v[82:83], v[94:95], v[82:83]
	v_pk_add_f32 v[218:219], v[96:97], v[218:219]
	s_nop 0
	v_pk_add_f32 v[82:83], v[82:83], v[218:219]
	s_nop 0
	v_add_f32_e32 v2, v82, v83
	v_cvt_pk_bf16_f32 v82, v16, v17
	v_cvt_pk_bf16_f32 v83, v84, v85
	v_cvt_pk_bf16_f32 v84, v86, v87
	v_cvt_pk_bf16_f32 v85, v88, v89
	v_add_f32_e32 v144, v144, v2
	s_waitcnt lgkmcnt(0)
	s_setprio 1
	v_mfma_f32_32x32x16_bf16 v[66:81], v[118:121], v[82:85], v[66:81]
	v_mfma_f32_32x32x16_bf16 v[50:65], v[12:15], v[82:85], v[50:65]
	v_cvt_pk_bf16_f32 v12, v90, v91
	v_cvt_pk_bf16_f32 v13, v92, v93
	v_cvt_pk_bf16_f32 v14, v94, v95
	v_cvt_pk_bf16_f32 v15, v96, v97
	s_nop 0
	v_mfma_f32_32x32x16_bf16 v[66:81], v[8:11], v[12:15], v[66:81]
	v_mfma_f32_32x32x16_bf16 v[50:65], v[4:7], v[12:15], v[50:65]
	s_setprio 0

.LBB0_681:
	s_flbit_i32_b32 s0, s2
	s_xor_b32 s0, s0, 31
	s_lshl_b32 s8, 1, s0
	s_waitcnt lgkmcnt(0)
	v_and_b32_e32 v2, s8, v136
	v_cmp_ne_u32_e64 s[38:39], 0, v2
	s_mov_b64 vcc, s[38:39]
	s_cbranch_vccz .LBB0_669
	s_and_b32 s1, s5, 0xc000
	s_lshl_b32 s9, s0, 6
	s_lshr_b32 s0, s0, 2
	s_xor_b32 s1, s1, 0x8000
	v_cvt_f32_u32_e32 v159, s0
	s_add_i32 s1, s1, 0
	v_add_u32_e32 v2, s1, v137
	v_add_u32_e32 v4, s1, v138
	v_add_u32_e32 v5, s1, v139
	v_add_u32_e32 v6, s1, v140
	s_or_b32 s10, s9, 32
	s_cmp_gt_i32 s10, s6
	v_add_u32_e32 v163, v2, v134
	v_add_u32_e32 v162, v4, v134
	v_add_u32_e32 v161, v5, v134
	v_add_u32_e32 v160, v6, v134
	v_add_u32_e32 v17, s1, v156
	v_add_u32_e32 v16, s1, v157
	s_cbranch_scc1 .LBB0_690
	ds_read_b128 v[4:7], v163 offset:4096
	ds_read_b128 v[188:191], v162 offset:4096
	ds_read_b128 v[192:195], v161 offset:4096
	ds_read_b128 v[202:205], v160 offset:4096
	s_and_b32 s0, s10, 0xe0
	v_or_b32_e32 v2, s0, v129
	v_cvt_f32_ubyte0_e32 v2, v2
	v_and_b32_e32 v2, 0x7fff0000, v2
	v_or_b32_sdwa v2, v2, v159 dst_sel:DWORD dst_unused:UNUSED_PAD src0_sel:DWORD src1_sel:WORD_1
	v_cndmask_b32_e64 v210, 0, v2, s[22:23]
	s_or_b32 s0, s9, 63
	s_cmp_lt_u32 s16, s0
	s_waitcnt lgkmcnt(3)
	s_setprio 1
	v_mfma_f32_32x32x16_bf16 v[82:97], v[4:7], v[106:109], 0
	s_cselect_b64 s[0:1], -1, 0
	s_sub_i32 s11, s16, s10
	s_cmp_gt_i32 s11, 0x3fffffe0
	v_add3_u32 v164, v16, v135, s69
	s_cselect_b64 s[12:13], -1, 0
	s_or_b64 s[0:1], s[0:1], s[12:13]
	s_and_b64 vcc, exec, s[0:1]
	s_waitcnt lgkmcnt(2)
	v_mfma_f32_32x32x16_bf16 v[82:97], v[188:191], v[98:101], v[82:97]
	s_waitcnt lgkmcnt(1)
	v_mfma_f32_32x32x16_bf16 v[82:97], v[192:195], v[102:105], v[82:97]
	s_waitcnt lgkmcnt(0)
	v_mfma_f32_32x32x16_bf16 v[82:97], v[202:205], v[110:113], v[82:97]
	v_mfma_f32_32x32x16_bf16 v[82:97], v[210:213], v[114:117], v[82:97]
	v_add3_u32 v2, v17, v135, s69
	ds_read_b64_tr_b16 v[118:119], v2
	ds_read_b64_tr_b16 v[120:121], v2 offset:1024
	ds_read_b64_tr_b16 v[12:13], v164
	ds_read_b64_tr_b16 v[14:15], v164 offset:1024
	ds_read_b64_tr_b16 v[8:9], v2 offset:2048
	ds_read_b64_tr_b16 v[10:11], v2 offset:3072
	ds_read_b64_tr_b16 v[4:5], v164 offset:2048
	ds_read_b64_tr_b16 v[6:7], v164 offset:3072
	s_cbranch_vccnz .LBB0_685
	v_cndmask_b32_e64 v2, 0, 1, s[38:39]
	v_cmp_ne_u32_e32 vcc, 0, v2
	s_cmp_lg_u64 vcc, exec
	s_cselect_b64 s[0:1], -1, 0
	s_cbranch_scc0 .LBB0_687
	v_cndmask_b32_e64 v82, v197, v82, s[38:39]
	v_cndmask_b32_e64 v83, v197, v83, s[38:39]
	v_cndmask_b32_e64 v84, v197, v84, s[38:39]
	v_cndmask_b32_e64 v85, v197, v85, s[38:39]
	v_cndmask_b32_e64 v86, v197, v86, s[38:39]
	v_cndmask_b32_e64 v87, v197, v87, s[38:39]
	v_cndmask_b32_e64 v88, v197, v88, s[38:39]
	v_cndmask_b32_e64 v89, v197, v89, s[38:39]
	v_cndmask_b32_e64 v90, v197, v90, s[38:39]
	v_cndmask_b32_e64 v91, v197, v91, s[38:39]
	v_cndmask_b32_e64 v92, v197, v92, s[38:39]
	v_cndmask_b32_e64 v93, v197, v93, s[38:39]
	v_cndmask_b32_e64 v94, v197, v94, s[38:39]
	v_cndmask_b32_e64 v95, v197, v95, s[38:39]
	v_cndmask_b32_e64 v96, v197, v96, s[38:39]
	v_cndmask_b32_e64 v97, v197, v97, s[38:39]
	s_branch .LBB0_687

.LBB0_689:
	s_setprio 0
	v_mul_f32_e32 v2, 0xbfb8aa3b, v158
	v_fmamk_f32 v82, v82, 0x3fb8aa3b, v2
	v_fmamk_f32 v83, v83, 0x3fb8aa3b, v2
	v_exp_f32_e32 v82, v82
	v_exp_f32_e32 v83, v83
	v_fmamk_f32 v84, v84, 0x3fb8aa3b, v2
	v_fmamk_f32 v85, v85, 0x3fb8aa3b, v2
	v_exp_f32_e32 v84, v84
	v_exp_f32_e32 v85, v85
	v_fmamk_f32 v86, v86, 0x3fb8aa3b, v2
	v_fmamk_f32 v87, v87, 0x3fb8aa3b, v2
	v_fmamk_f32 v88, v88, 0x3fb8aa3b, v2
	v_fmamk_f32 v89, v89, 0x3fb8aa3b, v2
	v_pk_add_f32 v[164:165], v[82:83], 0 op_sel_hi:[1,0]
	v_exp_f32_e32 v86, v86
	v_exp_f32_e32 v87, v87
	v_exp_f32_e32 v88, v88
	v_exp_f32_e32 v89, v89
	v_pk_add_f32 v[164:165], v[84:85], v[164:165]
	v_cvt_pk_bf16_f32 v82, v82, v83
	v_cvt_pk_bf16_f32 v83, v84, v85
	v_cvt_pk_bf16_f32 v84, v86, v87
	v_cvt_pk_bf16_f32 v85, v88, v89
	v_fmamk_f32 v90, v90, 0x3fb8aa3b, v2
	s_waitcnt lgkmcnt(0)
	s_setprio 1
	v_mfma_f32_32x32x16_bf16 v[66:81], v[118:121], v[82:85], v[66:81]
	v_fmamk_f32 v91, v91, 0x3fb8aa3b, v2
	v_exp_f32_e32 v90, v90
	v_exp_f32_e32 v91, v91
	v_fmamk_f32 v92, v92, 0x3fb8aa3b, v2
	v_fmamk_f32 v93, v93, 0x3fb8aa3b, v2
	v_exp_f32_e32 v92, v92
	v_exp_f32_e32 v93, v93
	v_mfma_f32_32x32x16_bf16 v[50:65], v[12:15], v[82:85], v[50:65]
	v_fmamk_f32 v94, v94, 0x3fb8aa3b, v2
	v_fmamk_f32 v95, v95, 0x3fb8aa3b, v2
	v_fmamk_f32 v96, v96, 0x3fb8aa3b, v2
	v_fmac_f32_e32 v2, 0x3fb8aa3b, v97
	v_exp_f32_e32 v94, v94
	v_exp_f32_e32 v95, v95
	v_exp_f32_e32 v96, v96
	v_exp_f32_e32 v97, v2
	v_pk_add_f32 v[164:165], v[86:87], v[164:165]
	v_cvt_pk_bf16_f32 v12, v90, v91
	v_cvt_pk_bf16_f32 v13, v92, v93
	v_cvt_pk_bf16_f32 v14, v94, v95
	v_cvt_pk_bf16_f32 v15, v96, v97
	s_nop 0
	v_mfma_f32_32x32x16_bf16 v[66:81], v[8:11], v[12:15], v[66:81]
	v_add_f32_e64 v164, v88, v164
	v_add_f32_e64 v165, v89, v165
	v_add_f32_e64 v164, v90, v164
	v_add_f32_e64 v165, v91, v165
	v_add_f32_e64 v164, v92, v164
	v_add_f32_e64 v165, v93, v165
	v_pk_add_f32 v[164:165], v[94:95], v[164:165]
	v_mfma_f32_32x32x16_bf16 v[50:65], v[4:7], v[12:15], v[50:65]
	s_setprio 0
	v_add_f32_e64 v164, v96, v164
	v_add_f32_e64 v165, v97, v165
	v_add_f32_e32 v2, v164, v165
	v_add_f32_e32 v144, v144, v2
.LBB0_690:
	s_cmp_gt_i32 s9, s6
	s_cbranch_scc1 .LBB0_669
	ds_read_b128 v[4:7], v163
	ds_read_b128 v[188:191], v162
	ds_read_b128 v[192:195], v161
	ds_read_b128 v[202:205], v160
	s_and_b32 s0, s9, 0xc0
	v_or_b32_e32 v2, s0, v129
	v_cvt_f32_ubyte0_e32 v2, v2
	v_and_b32_e32 v2, 0x7fff0000, v2
	v_or_b32_sdwa v2, v2, v159 dst_sel:DWORD dst_unused:UNUSED_PAD src0_sel:DWORD src1_sel:WORD_1
	v_cndmask_b32_e64 v210, 0, v2, s[22:23]
	s_or_b32 s0, s9, 31
	s_cmp_lt_i32 s16, s0
	s_waitcnt lgkmcnt(3)
	s_setprio 1
	v_mfma_f32_32x32x16_bf16 v[82:97], v[4:7], v[106:109], 0
	s_cselect_b64 s[0:1], -1, 0
	s_sub_i32 s10, s16, s9
	s_cmp_gt_i32 s10, 0x3fffffe0
	v_add3_u32 v16, v16, v135, s67
	s_cselect_b64 s[10:11], -1, 0
	s_or_b64 s[0:1], s[0:1], s[10:11]
	s_and_b64 vcc, exec, s[0:1]
	s_waitcnt lgkmcnt(2)
	v_mfma_f32_32x32x16_bf16 v[82:97], v[188:191], v[98:101], v[82:97]
	s_waitcnt lgkmcnt(1)
	v_mfma_f32_32x32x16_bf16 v[82:97], v[192:195], v[102:105], v[82:97]
	s_waitcnt lgkmcnt(0)
	v_mfma_f32_32x32x16_bf16 v[82:97], v[202:205], v[110:113], v[82:97]
	v_mfma_f32_32x32x16_bf16 v[82:97], v[210:213], v[114:117], v[82:97]
	v_add3_u32 v2, v17, v135, s67
	ds_read_b64_tr_b16 v[118:119], v2
	ds_read_b64_tr_b16 v[120:121], v2 offset:1024
	ds_read_b64_tr_b16 v[12:13], v16
	ds_read_b64_tr_b16 v[14:15], v16 offset:1024
	ds_read_b64_tr_b16 v[8:9], v2 offset:2048
	ds_read_b64_tr_b16 v[10:11], v2 offset:3072
	ds_read_b64_tr_b16 v[4:5], v16 offset:2048
	ds_read_b64_tr_b16 v[6:7], v16 offset:3072
	s_cbranch_vccnz .LBB0_693
	v_cndmask_b32_e64 v2, 0, 1, s[38:39]
	v_cmp_ne_u32_e32 vcc, 0, v2
	s_cmp_lg_u64 vcc, exec
	s_cselect_b64 s[0:1], -1, 0
	s_cbranch_scc0 .LBB0_695
	v_cndmask_b32_e64 v82, v197, v82, s[38:39]
	v_cndmask_b32_e64 v83, v197, v83, s[38:39]
	v_cndmask_b32_e64 v84, v197, v84, s[38:39]
	v_cndmask_b32_e64 v85, v197, v85, s[38:39]
	v_cndmask_b32_e64 v86, v197, v86, s[38:39]
	v_cndmask_b32_e64 v87, v197, v87, s[38:39]
	v_cndmask_b32_e64 v88, v197, v88, s[38:39]
	v_cndmask_b32_e64 v89, v197, v89, s[38:39]
	v_cndmask_b32_e64 v90, v197, v90, s[38:39]
	v_cndmask_b32_e64 v91, v197, v91, s[38:39]
	v_cndmask_b32_e64 v92, v197, v92, s[38:39]
	v_cndmask_b32_e64 v93, v197, v93, s[38:39]
	v_cndmask_b32_e64 v94, v197, v94, s[38:39]
	v_cndmask_b32_e64 v95, v197, v95, s[38:39]
	v_cndmask_b32_e64 v96, v197, v96, s[38:39]
	v_cndmask_b32_e64 v97, v197, v97, s[38:39]
	s_branch .LBB0_695

.LBB0_770:
	s_setprio 0
	v_mul_f32_e32 v2, 0xbfb8aa3b, v113
	v_fmamk_f32 v16, v50, 0x3fb8aa3b, v2
	v_fmamk_f32 v50, v52, 0x3fb8aa3b, v2
	v_exp_f32_e32 v52, v50
	v_fmamk_f32 v50, v53, 0x3fb8aa3b, v2
	v_exp_f32_e32 v53, v50
	v_fmamk_f32 v50, v54, 0x3fb8aa3b, v2
	v_exp_f32_e32 v54, v50
	v_fmamk_f32 v50, v55, 0x3fb8aa3b, v2
	v_exp_f32_e32 v55, v50
	v_fmamk_f32 v50, v56, 0x3fb8aa3b, v2
	v_exp_f32_e32 v56, v50
	v_fmamk_f32 v50, v57, 0x3fb8aa3b, v2
	v_exp_f32_e32 v57, v50
	v_fmamk_f32 v50, v58, 0x3fb8aa3b, v2
	v_exp_f32_e32 v58, v50
	v_fmamk_f32 v50, v59, 0x3fb8aa3b, v2
	v_fmamk_f32 v17, v51, 0x3fb8aa3b, v2
	v_exp_f32_e32 v59, v50
	v_fmamk_f32 v50, v60, 0x3fb8aa3b, v2
	v_exp_f32_e32 v16, v16
	v_exp_f32_e32 v17, v17
	v_exp_f32_e32 v60, v50
	v_fmamk_f32 v50, v61, 0x3fb8aa3b, v2
	v_exp_f32_e32 v61, v50
	v_fmamk_f32 v50, v62, 0x3fb8aa3b, v2
	v_exp_f32_e32 v62, v50
	v_fmamk_f32 v50, v63, 0x3fb8aa3b, v2
	v_exp_f32_e32 v63, v50
	v_fmamk_f32 v50, v64, 0x3fb8aa3b, v2
	v_exp_f32_e32 v64, v50
	v_fmac_f32_e32 v2, 0x3fb8aa3b, v65
	v_pk_add_f32 v[50:51], v[16:17], v[52:53]
	v_exp_f32_e32 v65, v2
	v_pk_add_f32 v[244:245], v[54:55], v[56:57]
	v_pk_add_f32 v[50:51], v[58:59], v[50:51]
	v_pk_add_f32 v[244:245], v[60:61], v[244:245]
	v_pk_add_f32 v[50:51], v[62:63], v[50:51]
	v_pk_add_f32 v[244:245], v[64:65], v[244:245]
	s_nop 0
	v_pk_add_f32 v[50:51], v[50:51], v[244:245]
	s_nop 0
	v_add_f32_e32 v2, v50, v51
	v_cvt_pk_bf16_f32 v50, v16, v17
	v_cvt_pk_bf16_f32 v51, v52, v53
	v_cvt_pk_bf16_f32 v52, v54, v55
	v_cvt_pk_bf16_f32 v53, v56, v57
	v_add_f32_e32 v108, v108, v2
	s_waitcnt lgkmcnt(0)
	s_setprio 1
	v_mfma_f32_32x32x16_bf16 v[34:49], v[86:89], v[50:53], v[34:49]
	v_mfma_f32_32x32x16_bf16 v[18:33], v[12:15], v[50:53], v[18:33]
	v_cvt_pk_bf16_f32 v12, v58, v59
	v_cvt_pk_bf16_f32 v13, v60, v61
	v_cvt_pk_bf16_f32 v14, v62, v63
	v_cvt_pk_bf16_f32 v15, v64, v65
	s_nop 0
	v_mfma_f32_32x32x16_bf16 v[34:49], v[8:11], v[12:15], v[34:49]
	v_mfma_f32_32x32x16_bf16 v[18:33], v[4:7], v[12:15], v[18:33]
	s_setprio 0

.Lw_swa_4_done:
.LBB0_780:
	s_cmp_eq_u32 s32, 0
	s_cselect_b32 s84, 0, 1
	s_sub_u32 s32, s32, s84
	s_add_i32 s0, s25, s17
	s_add_i32 s1, s23, s18
	s_add_i32 s1, s1, -1
	s_and_b32 s27, s26, 0xc000
	s_add_i32 s34, s27, 0
	s_ashr_i32 s1, s1, 2
	s_add_i32 s27, s0, 0x7e0
	s_cmp_gt_i32 s27, s19
	v_cvt_f32_i32_e32 v114, s1
	s_cselect_b64 s[28:29], -1, 0
	s_add_i32 s1, s0, 0x7ff
	s_cmp_lt_i32 s1, s20
	s_cselect_b64 s[30:31], -1, 0
	v_add_u32_e32 v2, s34, v104
	v_add_u32_e32 v4, s34, v105
	v_add_u32_e32 v5, s34, v106
	v_add_u32_e32 v6, s34, v107
	s_or_b64 s[28:29], s[28:29], s[30:31]
	s_and_b64 vcc, exec, s[28:29]
	v_add_u32_e32 v118, v2, v103
	v_add_u32_e32 v117, v4, v103
	v_add_u32_e32 v116, v5, v103
	v_add_u32_e32 v115, v6, v103
	v_add_u32_e32 v16, s34, v109
	v_add_u32_e32 v17, s34, v110
	s_barrier
	s_cbranch_vccnz .LBB0_788
	ds_read_b128 v[4:7], v118 offset:4096
	ds_read_b128 v[188:191], v117 offset:4096
	ds_read_b128 v[192:195], v116 offset:4096
	ds_read_b128 v[202:205], v115 offset:4096
	s_and_b32 s27, s27, 0xe0
	v_or_b32_e32 v2, s27, v102
	v_cvt_f32_ubyte0_e32 v2, v2
	v_and_b32_e32 v2, 0x7fff0000, v2
	v_or_b32_sdwa v2, v2, v114 dst_sel:DWORD dst_unused:UNUSED_PAD src0_sel:DWORD src1_sel:WORD_1
	v_cndmask_b32_e64 v246, 0, v2, s[36:37]
	s_cmp_ge_i32 s16, s1
	s_cselect_b64 s[28:29], -1, 0
	s_waitcnt lgkmcnt(3)
	s_setprio 1
	v_mfma_f32_32x32x16_bf16 v[50:65], v[4:7], v[66:69], 0
	s_sub_i32 s1, s15, 32
	s_cmpk_lt_i32 s1, 0x61
	v_add3_u32 v119, v17, v96, s69
	s_cselect_b64 s[30:31], -1, 0
	s_and_b64 s[28:29], s[28:29], s[30:31]
	s_and_b64 vcc, exec, s[28:29]
	s_waitcnt lgkmcnt(2)
	v_mfma_f32_32x32x16_bf16 v[50:65], v[188:191], v[70:73], v[50:65]
	s_waitcnt lgkmcnt(1)
	v_mfma_f32_32x32x16_bf16 v[50:65], v[192:195], v[74:77], v[50:65]
	s_waitcnt lgkmcnt(0)
	v_mfma_f32_32x32x16_bf16 v[50:65], v[202:205], v[78:81], v[50:65]
	v_mfma_f32_32x32x16_bf16 v[50:65], v[246:249], v[82:85], v[50:65]
	v_add3_u32 v2, v16, v96, s69
	ds_read_b64_tr_b16 v[86:87], v2
	ds_read_b64_tr_b16 v[88:89], v2 offset:1024
	ds_read_b64_tr_b16 v[12:13], v119
	ds_read_b64_tr_b16 v[14:15], v119 offset:1024
	ds_read_b64_tr_b16 v[8:9], v2 offset:2048
	ds_read_b64_tr_b16 v[10:11], v2 offset:3072
	ds_read_b64_tr_b16 v[4:5], v119 offset:2048
	ds_read_b64_tr_b16 v[6:7], v119 offset:3072
	s_cbranch_vccnz .LBB0_785
	v_add_u32_e32 v2, s15, v111
	v_subrev_u32_e32 v119, 32, v2
	v_cmp_gt_u32_e32 vcc, s71, v119
	v_add3_u32 v119, v112, s17, 32
	s_nop 5
	v_cndmask_b32_e32 v50, v197, v50, vcc
	v_cmp_lt_u32_e32 vcc, s47, v119
	v_subrev_u32_e32 v119, 34, v2
	s_nop 0
	v_cndmask_b32_e32 v51, v197, v51, vcc
	v_cmp_gt_u32_e32 vcc, s71, v119
	v_subrev_u32_e32 v119, 35, v2
	s_nop 0
	v_cndmask_b32_e32 v52, v197, v52, vcc
	v_cmp_gt_u32_e32 vcc, s71, v119
	v_subrev_u32_e32 v119, 40, v2
	s_nop 0
	v_cndmask_b32_e32 v53, v197, v53, vcc
	v_cmp_gt_u32_e32 vcc, s71, v119
	v_subrev_u32_e32 v119, 41, v2
	s_nop 0
	v_cndmask_b32_e32 v54, v197, v54, vcc
	v_cmp_gt_u32_e32 vcc, s71, v119
	v_subrev_u32_e32 v119, 42, v2
	s_nop 0
	v_cndmask_b32_e32 v55, v197, v55, vcc
	v_cmp_gt_u32_e32 vcc, s71, v119
	v_subrev_u32_e32 v119, 43, v2
	s_nop 0
	v_cndmask_b32_e32 v56, v197, v56, vcc
	v_cmp_gt_u32_e32 vcc, s71, v119
	v_subrev_u32_e32 v119, 48, v2
	s_nop 0
	v_cndmask_b32_e32 v57, v197, v57, vcc
	v_cmp_gt_u32_e32 vcc, s71, v119
	v_subrev_u32_e32 v119, 49, v2
	s_nop 0
	v_cndmask_b32_e32 v58, v197, v58, vcc
	v_cmp_gt_u32_e32 vcc, s71, v119
	v_subrev_u32_e32 v119, 50, v2
	s_nop 0
	v_cndmask_b32_e32 v59, v197, v59, vcc
	v_cmp_gt_u32_e32 vcc, s71, v119
	v_subrev_u32_e32 v119, 51, v2
	s_nop 0
	v_cndmask_b32_e32 v60, v197, v60, vcc
	v_cmp_gt_u32_e32 vcc, s71, v119
	v_subrev_u32_e32 v119, 56, v2
	s_nop 0
	v_cndmask_b32_e32 v61, v197, v61, vcc
	v_cmp_gt_u32_e32 vcc, s71, v119
	v_subrev_u32_e32 v119, 57, v2
	s_nop 0
	v_cndmask_b32_e32 v62, v197, v62, vcc
	v_cmp_gt_u32_e32 vcc, s71, v119
	v_subrev_u32_e32 v119, 58, v2
	v_subrev_u32_e32 v2, 59, v2
	v_cndmask_b32_e32 v63, v197, v63, vcc
	v_cmp_gt_u32_e32 vcc, s71, v119
	s_nop 1
	v_cndmask_b32_e32 v64, v197, v64, vcc
	v_cmp_gt_u32_e32 vcc, s71, v2
	s_nop 1
	v_cndmask_b32_e32 v65, v197, v65, vcc

.LBB0_787:
	s_setprio 0
	v_mul_f32_e32 v2, 0xbfb8aa3b, v113
	v_fmamk_f32 v50, v50, 0x3fb8aa3b, v2
	v_fmamk_f32 v51, v51, 0x3fb8aa3b, v2
	v_exp_f32_e32 v50, v50
	v_exp_f32_e32 v51, v51
	v_fmamk_f32 v52, v52, 0x3fb8aa3b, v2
	v_fmamk_f32 v53, v53, 0x3fb8aa3b, v2
	v_exp_f32_e32 v52, v52
	v_exp_f32_e32 v53, v53
	v_fmamk_f32 v54, v54, 0x3fb8aa3b, v2
	v_fmamk_f32 v55, v55, 0x3fb8aa3b, v2
	v_fmamk_f32 v56, v56, 0x3fb8aa3b, v2
	v_fmamk_f32 v57, v57, 0x3fb8aa3b, v2
	v_pk_add_f32 v[120:121], v[50:51], 0 op_sel_hi:[1,0]
	v_exp_f32_e32 v54, v54
	v_exp_f32_e32 v55, v55
	v_exp_f32_e32 v56, v56
	v_exp_f32_e32 v57, v57
	v_pk_add_f32 v[120:121], v[52:53], v[120:121]
	v_cvt_pk_bf16_f32 v50, v50, v51
	v_cvt_pk_bf16_f32 v51, v52, v53
	v_cvt_pk_bf16_f32 v52, v54, v55
	v_cvt_pk_bf16_f32 v53, v56, v57
	v_fmamk_f32 v58, v58, 0x3fb8aa3b, v2
	s_waitcnt lgkmcnt(0)
	s_setprio 1
	v_mfma_f32_32x32x16_bf16 v[34:49], v[86:89], v[50:53], v[34:49]
	v_fmamk_f32 v59, v59, 0x3fb8aa3b, v2
	v_exp_f32_e32 v58, v58
	v_exp_f32_e32 v59, v59
	v_fmamk_f32 v60, v60, 0x3fb8aa3b, v2
	v_fmamk_f32 v61, v61, 0x3fb8aa3b, v2
	v_exp_f32_e32 v60, v60
	v_exp_f32_e32 v61, v61
	v_mfma_f32_32x32x16_bf16 v[18:33], v[12:15], v[50:53], v[18:33]
	v_fmamk_f32 v62, v62, 0x3fb8aa3b, v2
	v_fmamk_f32 v63, v63, 0x3fb8aa3b, v2
	v_fmamk_f32 v64, v64, 0x3fb8aa3b, v2
	v_fmac_f32_e32 v2, 0x3fb8aa3b, v65
	v_exp_f32_e32 v62, v62
	v_exp_f32_e32 v63, v63
	v_exp_f32_e32 v64, v64
	v_exp_f32_e32 v65, v2
	v_pk_add_f32 v[120:121], v[54:55], v[120:121]
	v_cvt_pk_bf16_f32 v12, v58, v59
	v_cvt_pk_bf16_f32 v13, v60, v61
	v_cvt_pk_bf16_f32 v14, v62, v63
	v_cvt_pk_bf16_f32 v15, v64, v65
	s_nop 0
	v_mfma_f32_32x32x16_bf16 v[34:49], v[8:11], v[12:15], v[34:49]
	v_add_f32_e64 v120, v56, v120
	v_add_f32_e64 v121, v57, v121
	v_add_f32_e64 v120, v58, v120
	v_add_f32_e64 v121, v59, v121
	v_add_f32_e64 v120, v60, v120
	v_add_f32_e64 v121, v61, v121
	v_pk_add_f32 v[120:121], v[62:63], v[120:121]
	v_mfma_f32_32x32x16_bf16 v[18:33], v[4:7], v[12:15], v[18:33]
	s_setprio 0
	v_add_f32_e64 v120, v64, v120
	v_add_f32_e64 v121, v65, v121
	v_add_f32_e32 v2, v120, v121
	v_add_f32_e32 v108, v108, v2

.Lring_issue_skip_1:
	s_add_i32 s1, s0, 0x7c0
	s_cmp_gt_i32 s1, s19
	s_cselect_b64 s[28:29], -1, 0
	s_addk_i32 s0, 0x7df
	s_cmp_lt_i32 s0, s20
	s_cselect_b64 s[30:31], -1, 0
	s_or_b64 s[28:29], s[28:29], s[30:31]
	s_and_b64 vcc, exec, s[28:29]
	s_cbranch_vccnz .LBB0_771
	ds_read_b128 v[4:7], v118
	ds_read_b128 v[188:191], v117
	ds_read_b128 v[192:195], v116
	ds_read_b128 v[202:205], v115
	s_and_b32 s1, s1, 0xc0
	v_or_b32_e32 v2, s1, v102
	v_cvt_f32_ubyte0_e32 v2, v2
	v_and_b32_e32 v2, 0x7fff0000, v2
	v_or_b32_sdwa v2, v2, v114 dst_sel:DWORD dst_unused:UNUSED_PAD src0_sel:DWORD src1_sel:WORD_1
	v_cndmask_b32_e64 v246, 0, v2, s[36:37]
	s_cmp_ge_i32 s16, s0
	s_cselect_b64 s[0:1], -1, 0
	s_waitcnt lgkmcnt(3)
	s_setprio 1
	v_mfma_f32_32x32x16_bf16 v[50:65], v[4:7], v[66:69], 0
	s_cmpk_lt_i32 s15, 0x61
	s_cselect_b64 s[28:29], -1, 0
	s_and_b64 s[0:1], s[0:1], s[28:29]
	s_and_b64 vcc, exec, s[0:1]
	s_waitcnt lgkmcnt(2)
	v_mfma_f32_32x32x16_bf16 v[50:65], v[188:191], v[70:73], v[50:65]
	s_waitcnt lgkmcnt(1)
	v_mfma_f32_32x32x16_bf16 v[50:65], v[192:195], v[74:77], v[50:65]
	s_waitcnt lgkmcnt(0)
	v_mfma_f32_32x32x16_bf16 v[50:65], v[202:205], v[78:81], v[50:65]
	v_mfma_f32_32x32x16_bf16 v[50:65], v[246:249], v[82:85], v[50:65]
	v_add3_u32 v2, v16, v96, s67
	v_add3_u32 v16, v17, v96, s67
	ds_read_b64_tr_b16 v[86:87], v2
	ds_read_b64_tr_b16 v[88:89], v2 offset:1024
	ds_read_b64_tr_b16 v[12:13], v16
	ds_read_b64_tr_b16 v[14:15], v16 offset:1024
	ds_read_b64_tr_b16 v[8:9], v2 offset:2048
	ds_read_b64_tr_b16 v[10:11], v2 offset:3072
	ds_read_b64_tr_b16 v[4:5], v16 offset:2048
	ds_read_b64_tr_b16 v[6:7], v16 offset:3072
	s_cbranch_vccnz .LBB0_791
	v_add_u32_e32 v2, s15, v111
	v_cmp_gt_u32_e32 vcc, s71, v2
	v_add_u32_e32 v16, s17, v112
	s_nop 5
	v_cndmask_b32_e32 v50, v197, v50, vcc
	v_cmp_lt_u32_e32 vcc, s47, v16
	v_add_u32_e32 v16, -2, v2
	s_nop 0
	v_cndmask_b32_e32 v51, v197, v51, vcc
	v_cmp_gt_u32_e32 vcc, s71, v16
	v_add_u32_e32 v16, -3, v2
	s_nop 0
	v_cndmask_b32_e32 v52, v197, v52, vcc
	v_cmp_gt_u32_e32 vcc, s71, v16
	v_add_u32_e32 v16, -8, v2
	s_nop 0
	v_cndmask_b32_e32 v53, v197, v53, vcc
	v_cmp_gt_u32_e32 vcc, s71, v16
	v_add_u32_e32 v16, -9, v2
	s_nop 0
	v_cndmask_b32_e32 v54, v197, v54, vcc
	v_cmp_gt_u32_e32 vcc, s71, v16
	v_add_u32_e32 v16, -10, v2
	s_nop 0
	v_cndmask_b32_e32 v55, v197, v55, vcc
	v_cmp_gt_u32_e32 vcc, s71, v16
	v_add_u32_e32 v16, -11, v2
	s_nop 0
	v_cndmask_b32_e32 v56, v197, v56, vcc
	v_cmp_gt_u32_e32 vcc, s71, v16
	v_add_u32_e32 v16, -16, v2
	s_nop 0
	v_cndmask_b32_e32 v57, v197, v57, vcc
	v_cmp_gt_u32_e32 vcc, s71, v16
	v_subrev_u32_e32 v16, 17, v2
	s_nop 0
	v_cndmask_b32_e32 v58, v197, v58, vcc
	v_cmp_gt_u32_e32 vcc, s71, v16
	v_subrev_u32_e32 v16, 18, v2
	s_nop 0
	v_cndmask_b32_e32 v59, v197, v59, vcc
	v_cmp_gt_u32_e32 vcc, s71, v16
	v_subrev_u32_e32 v16, 19, v2
	s_nop 0
	v_cndmask_b32_e32 v60, v197, v60, vcc
	v_cmp_gt_u32_e32 vcc, s71, v16
	v_subrev_u32_e32 v16, 24, v2
	s_nop 0
	v_cndmask_b32_e32 v61, v197, v61, vcc
	v_cmp_gt_u32_e32 vcc, s71, v16
	v_subrev_u32_e32 v16, 25, v2
	s_nop 0
	v_cndmask_b32_e32 v62, v197, v62, vcc
	v_cmp_gt_u32_e32 vcc, s71, v16
	v_subrev_u32_e32 v16, 26, v2
	v_subrev_u32_e32 v2, 27, v2
	v_cndmask_b32_e32 v63, v197, v63, vcc
	v_cmp_gt_u32_e32 vcc, s71, v16
	s_nop 1
	v_cndmask_b32_e32 v64, v197, v64, vcc
	v_cmp_gt_u32_e32 vcc, s71, v2
	s_nop 1
	v_cndmask_b32_e32 v65, v197, v65, vcc
